# slot table preset to -1 in the router phase; top-k redirects the stores of not-taken tokens to a dense scratch line (1/8 of the scattered line writes)
# baseline (speedup 1.0000x reference)
.LBB0_650:
	s_or_b64 exec, exec, s[0:1]
	v_readlane_b32 s100, v235, 0
	v_readlane_b32 s101, v235, 1
	s_lshl_b32 s99, s56, 12
	v_lshlrev_b32_e32 v236, 3, v186
	v_mov_b32_e32 v238, -1
	v_mov_b32_e32 v239, -1
	s_add_u32 s100, s100, s99
	s_addc_u32 s101, s101, 0
	s_add_u32 s100, s100, 0x15b000
	s_addc_u32 s101, s101, 0
	global_store_dwordx2 v236, v[238:239], s[100:101]
	v_readfirstlane_b32 s100, v186
	s_nop 0
	s_cmp_lg_u32 s100, 0
	s_cbranch_scc1 .Lp7_w_skip
	s_cmp_eq_u32 s98, 0
	s_cbranch_scc1 .Lp7_w_skip
	v_readlane_b32 s100, v235, 7
	v_readlane_b32 s101, v235, 8
	v_mov_b32_e32 v236, 0x3400
	v_mov_b32_e32 v239, 0
	s_nop 3

.LBB0_724:
	s_andn2_b64 vcc, exec, s[0:1]
	s_cbranch_vccnz .LBB0_919
	v_mov_b32_e32 v0, v186
	s_andn2_b64 vcc, exec, s[4:5]
	s_cbranch_vccnz .LBB0_919
	s_load_dwordx2 s[0:1], s[6:7], 0x98
	v_and_b32_e32 v2, 63, v0
	v_ashrrev_i32_e32 v1, 6, v0
	v_lshlrev_b32_e32 v20, 4, v0
	v_cmp_gt_u32_e64 s[6:7], 64, v0
	s_waitcnt lgkmcnt(0)
	s_add_u32 s30, s0, 0x11b000
	s_addc_u32 s31, s1, 0
	s_add_u32 s34, s0, 0x13b000
	s_addc_u32 s35, s1, 0
	s_add_u32 s2, s0, 0x15b000
	v_writelane_b32 v235, s2, 20
	s_addc_u32 s2, s1, 0
	v_writelane_b32 v235, s2, 21
	s_movk_i32 s2, 0x100
	v_cmp_gt_i32_e64 s[4:5], s2, v0
	v_cmp_eq_u32_e64 s[2:3], 0, v2
	v_lshlrev_b32_e32 v22, 2, v0
	v_mul_lo_u32 v3, v0, 12
	v_writelane_b32 v235, s2, 22
	v_mbcnt_hi_u32_b32 v0, -1, v187
	v_and_b32_e32 v5, 63, v0
	v_writelane_b32 v235, s3, 23
	v_cmp_gt_u32_e64 s[2:3], 2, v2
	v_cmp_ne_u32_e32 vcc, 63, v5
	v_and_b32_e32 v4, 64, v0
	v_writelane_b32 v235, s2, 24
	v_addc_co_u32_e32 v6, vcc, 0, v0, vcc
	s_nop 0
	v_writelane_b32 v235, s3, 25
	v_cmp_gt_u32_e64 s[2:3], 4, v2
	v_cmp_gt_u32_e32 vcc, 62, v5
	v_lshlrev_b32_e32 v36, 2, v6
	v_writelane_b32 v235, s2, 26
	v_cndmask_b32_e64 v6, 0, 2, vcc
	v_cmp_gt_u32_e32 vcc, 60, v5
	v_writelane_b32 v235, s3, 27
	v_cmp_gt_u32_e64 s[2:3], 8, v2
	v_add_lshl_u32 v37, v6, v0, 2
	v_cndmask_b32_e64 v6, 0, 4, vcc
	v_writelane_b32 v235, s2, 28
	v_cmp_gt_u32_e32 vcc, 56, v5
	v_add_lshl_u32 v38, v6, v0, 2
	v_writelane_b32 v235, s3, 29
	v_cmp_gt_u32_e64 s[2:3], 16, v2
	v_cndmask_b32_e64 v6, 0, 8, vcc
	v_cmp_gt_u32_e32 vcc, 48, v5
	v_writelane_b32 v235, s2, 30
	s_add_u32 s36, s0, 0x25b000
	v_cndmask_b32_e64 v5, 0, 16, vcc
	v_writelane_b32 v235, s3, 31
	v_cmp_lt_i32_e64 s[2:3], 0, v1
	v_add_lshl_u32 v40, v5, v0, 2
	v_mov_b32_e32 v5, 0x80
	v_writelane_b32 v235, s2, 32
	v_lshl_or_b32 v41, v0, 2, v5
	v_add_u32_e32 v5, -1, v0
	v_writelane_b32 v235, s3, 33
	v_cmp_lt_i32_e64 s[2:3], 1, v1
	v_cmp_lt_i32_e32 vcc, v5, v4
	s_addc_u32 s37, s1, 0
	v_writelane_b32 v235, s2, 34
	v_cndmask_b32_e32 v5, v5, v0, vcc
	v_lshlrev_b32_e32 v42, 2, v5
	v_writelane_b32 v235, s3, 35
	v_cmp_lt_i32_e64 s[2:3], 2, v1
	v_add_u32_e32 v5, -2, v0
	v_cmp_lt_i32_e32 vcc, v5, v4
	v_writelane_b32 v235, s2, 36
	v_cmp_eq_u32_e64 s[8:9], 63, v2
	v_cndmask_b32_e32 v5, v5, v0, vcc
	v_writelane_b32 v235, s3, 37
	v_cmp_lt_i32_e64 s[2:3], 3, v1
	v_lshlrev_b32_e32 v43, 2, v5
	v_add_u32_e32 v5, -4, v0
	v_writelane_b32 v235, s2, 38
	v_cmp_lt_i32_e32 vcc, v5, v4
	v_cmp_gt_u32_e64 s[10:11], 62, v2
	v_writelane_b32 v235, s3, 39
	v_cmp_lt_i32_e64 s[2:3], 4, v1
	v_cndmask_b32_e32 v5, v5, v0, vcc
	v_lshlrev_b32_e32 v44, 2, v5
	v_writelane_b32 v235, s2, 40
	v_add_u32_e32 v5, -8, v0
	v_cmp_lt_i32_e32 vcc, v5, v4
	v_writelane_b32 v235, s3, 41
	v_cmp_lt_i32_e64 s[2:3], 5, v1
	v_cndmask_b32_e32 v5, v5, v0, vcc
	v_lshlrev_b32_e32 v45, 2, v5
	v_writelane_b32 v235, s2, 42
	v_add_u32_e32 v5, -16, v0
	v_cmp_gt_u32_e64 s[12:13], 60, v2
	v_writelane_b32 v235, s3, 43
	v_cmp_lt_i32_e64 s[2:3], 6, v1
	v_cmp_gt_u32_e64 s[14:15], 56, v2
	v_cmp_gt_u32_e64 s[16:17], 48, v2
	v_writelane_b32 v235, s2, 44
	v_cmp_gt_u32_e64 s[18:19], 32, v2
	v_cmp_lt_i32_e32 vcc, v5, v4
	v_writelane_b32 v235, s3, 45
	v_cmp_lt_i32_e64 s[2:3], 7, v1
	v_subrev_u32_e32 v2, 32, v0
	v_cndmask_b32_e32 v5, v5, v0, vcc
	v_writelane_b32 v235, s2, 46
	v_cmp_lt_i32_e32 vcc, v2, v4
	v_ashrrev_i32_e32 v21, 31, v20
	v_writelane_b32 v235, s3, 47
	v_add_lshl_u32 v39, v6, v0, 2
	v_readlane_b32 s24, v235, 16
	v_readlane_b32 s20, v235, 0
	v_readlane_b32 s25, v235, 17
	v_readlane_b32 s22, v235, 2
	s_lshl_b32 s33, s24, 10
	s_lshl_b32 s47, s22, 10
	s_lshl_b64 s[2:3], s[24:25], 15
	s_add_u32 s0, s0, s2
	v_cndmask_b32_e32 v0, v2, v0, vcc
	s_addc_u32 s1, s1, s3
	v_lshl_add_u32 v35, v1, 2, 0
	v_lshlrev_b32_e32 v47, 2, v0
	v_lshl_add_u64 v[0:1], v[20:21], 2, s[0:1]
	s_mov_b64 s[0:1], 0x1b000
	v_add_u32_e32 v34, 0, v22
	v_lshl_add_u64 v[30:31], v[0:1], 0, s[0:1]
	s_ashr_i32 s1, s22, 31
	s_mov_b32 s0, s22
	v_or_b32_e32 v24, 3, v22
	v_or_b32_e32 v26, 2, v22
	v_or_b32_e32 v28, 1, v22
	v_lshlrev_b32_e32 v46, 2, v5
	v_or_b32_e32 v48, 1, v20
	v_or_b32_e32 v49, 2, v20
	v_or_b32_e32 v50, 3, v20
	v_or_b32_e32 v51, 4, v20
	v_or_b32_e32 v52, 5, v20
	v_or_b32_e32 v53, 6, v20
	v_or_b32_e32 v54, 7, v20
	v_or_b32_e32 v55, 8, v20
	v_or_b32_e32 v56, 9, v20
	v_or_b32_e32 v57, 10, v20
	v_or_b32_e32 v58, 11, v20
	v_or_b32_e32 v59, 12, v20
	v_or_b32_e32 v60, 13, v20
	v_or_b32_e32 v61, 14, v20
	v_or_b32_e32 v62, 15, v20
	s_lshl_b64 s[38:39], s[0:1], 15
	v_mov_b32_e32 v21, 0
	v_mov_b32_e32 v63, 1
	s_movk_i32 s42, 0x3ff
	v_add_u32_e32 v64, v34, v3
	s_mov_b32 s43, s24
	v_readlane_b32 s21, v235, 1
	v_readlane_b32 s23, v235, 3
	v_readlane_b32 s100, v235, 0
	v_readlane_b32 s101, v235, 1
	v_readlane_b32 s99, v235, 16
	v_and_b32_e32 v252, 63, v186
	v_lshlrev_b32_e32 v252, 2, v252
	v_mov_b32_e32 v253, 0
	s_lshl_b32 s99, s99, 8
	s_add_u32 s100, s100, s99
	s_addc_u32 s101, s101, 0
	s_add_u32 s100, s100, 0xf173000
	s_addc_u32 s101, s101, 0
	v_lshl_add_u64 v[252:253], s[100:101], 0, v[252:253]
	s_branch .LBB0_728
.LBB0_727:
	s_or_b64 exec, exec, s[0:1]
	v_add_u32_e32 v2, s28, v62
	v_readlane_b32 s0, v235, 0
	v_ashrrev_i32_e32 v3, 31, v2
	v_readlane_b32 s2, v235, 2
	v_lshlrev_b64 v[2:3], 6, v[2:3]
	s_add_i32 s43, s43, s2
	s_add_i32 s33, s33, s47
	v_lshl_add_u64 v[2:3], s[26:27], 0, v[2:3]
	s_cmp_gt_i32 s43, 31
	v_lshl_add_u64 v[30:31], v[30:31], 0, s[38:39]
	v_cmp_ne_u32_e64 s[100:101], -1, v0
	s_nop 1
	v_cndmask_b32_e64 v254, v252, v2, s[100:101]
	v_cndmask_b32_e64 v255, v253, v3, s[100:101]
	global_store_dword v[254:255], v0, off
	v_readlane_b32 s1, v235, 1
	v_readlane_b32 s3, v235, 3
	s_cbranch_scc1 .LBB0_918

.LBB0_888:
	s_or_b64 exec, exec, vcc
	v_cndmask_b32_e64 v12, 0, 1, s[26:27]
	v_cndmask_b32_e64 v75, 0, 1, s[28:29]
	s_lshl_b32 s28, s46, 13
	s_lshl_b32 s26, s45, 2
	v_readlane_b32 s27, v235, 20
	v_add_u32_e32 v76, s28, v20
	v_add_u32_sdwa v12, v73, v12 dst_sel:DWORD dst_unused:UNUSED_PAD src0_sel:WORD_0 src1_sel:DWORD
	v_add_u32_sdwa v73, sext(v73), v75 dst_sel:DWORD dst_unused:UNUSED_PAD src0_sel:WORD_1 src1_sel:DWORD
	s_add_u32 s26, s27, s26
	v_readlane_b32 s27, v235, 21
	v_ashrrev_i32_e32 v77, 31, v76
	v_cmp_lt_i32_e32 vcc, v73, v17
	s_addc_u32 s27, s27, 0
	v_lshlrev_b64 v[76:77], 6, v[76:77]
	s_and_b64 s[24:25], s[24:25], vcc
	v_lshl_add_u64 v[76:77], s[26:27], 0, v[76:77]
	s_or_b64 s[24:25], s[2:3], s[24:25]
	v_cmp_ne_u32_e64 s[100:101], -1, v74
	s_nop 1
	v_cndmask_b32_e64 v254, v252, v76, s[100:101]
	v_cndmask_b32_e64 v255, v253, v77, s[100:101]
	global_store_dword v[254:255], v74, off
	s_and_saveexec_b64 s[2:3], s[24:25]
	s_cbranch_execz .LBB0_890
	v_min_i32_e32 v72, v73, v17
	v_add_u32_e32 v72, v72, v12
	v_add_u32_e32 v74, s33, v72
	v_ashrrev_i32_e32 v75, 31, v74
	v_lshlrev_b64 v[74:75], 2, v[74:75]
	v_lshl_add_u64 v[76:77], s[30:31], 0, v[74:75]
	v_lshl_add_u64 v[74:75], s[34:35], 0, v[74:75]
	global_store_dword v[74:75], v13, off
	v_add_u32_e32 v74, s44, v72
	v_ashrrev_i32_e32 v75, 31, v74
	v_lshl_add_u64 v[74:75], v[74:75], 2, s[36:37]
	global_store_dword v[76:77], v48, off
	global_store_dword v[74:75], v13, off
.LBB0_890:
	s_or_b64 exec, exec, s[2:3]
	v_add_u32_e32 v74, s28, v48
	v_add_u32_e32 v13, v12, v70
	v_add_u32_e32 v70, v73, v71
	v_ashrrev_i32_e32 v75, 31, v74
	v_cmp_lt_i32_e32 vcc, v70, v17
	v_lshlrev_b64 v[74:75], 6, v[74:75]
	s_and_b64 s[0:1], s[0:1], vcc
	v_lshl_add_u64 v[74:75], s[26:27], 0, v[74:75]
	s_or_b64 s[2:3], s[20:21], s[0:1]
	v_mov_b32_e32 v12, -1
	v_mov_b32_e32 v71, -1
	v_cmp_ne_u32_e64 s[100:101], -1, v72
	s_nop 1
	v_cndmask_b32_e64 v254, v252, v74, s[100:101]
	v_cndmask_b32_e64 v255, v253, v75, s[100:101]
	global_store_dword v[254:255], v72, off
	s_and_saveexec_b64 s[0:1], s[2:3]
	s_cbranch_execz .LBB0_892
	v_min_i32_e32 v71, v70, v17
	v_add_u32_e32 v71, v71, v13
	v_add_u32_e32 v72, s33, v71
	v_ashrrev_i32_e32 v73, 31, v72
	v_lshlrev_b64 v[72:73], 2, v[72:73]
	v_lshl_add_u64 v[74:75], s[30:31], 0, v[72:73]
	v_lshl_add_u64 v[72:73], s[34:35], 0, v[72:73]
	global_store_dword v[72:73], v14, off
	v_add_u32_e32 v72, s44, v71
	v_ashrrev_i32_e32 v73, 31, v72
	v_lshl_add_u64 v[72:73], v[72:73], 2, s[36:37]
	global_store_dword v[74:75], v49, off
	global_store_dword v[72:73], v14, off
.LBB0_892:
	s_or_b64 exec, exec, s[0:1]
	v_add_u32_e32 v72, s28, v49
	v_add_u32_e32 v14, v70, v69
	v_ashrrev_i32_e32 v73, 31, v72
	v_cmp_lt_i32_e32 vcc, v14, v17
	v_lshlrev_b64 v[72:73], 6, v[72:73]
	s_and_b64 s[0:1], s[22:23], vcc
	v_lshl_add_u64 v[72:73], s[26:27], 0, v[72:73]
	v_add_u32_e32 v13, v13, v68
	s_or_b64 s[2:3], s[96:97], s[0:1]
	v_cmp_ne_u32_e64 s[100:101], -1, v71
	s_nop 1
	v_cndmask_b32_e64 v254, v252, v72, s[100:101]
	v_cndmask_b32_e64 v255, v253, v73, s[100:101]
	global_store_dword v[254:255], v71, off
	s_and_saveexec_b64 s[0:1], s[2:3]
	s_cbranch_execz .LBB0_894
	v_min_i32_e32 v12, v14, v17
	v_add_u32_e32 v12, v12, v13
	v_add_u32_e32 v68, s33, v12
	v_ashrrev_i32_e32 v69, 31, v68
	v_lshlrev_b64 v[68:69], 2, v[68:69]
	v_lshl_add_u64 v[70:71], s[30:31], 0, v[68:69]
	v_lshl_add_u64 v[68:69], s[34:35], 0, v[68:69]
	global_store_dword v[68:69], v15, off
	v_add_u32_e32 v68, s44, v12
	v_ashrrev_i32_e32 v69, 31, v68
	v_lshl_add_u64 v[68:69], v[68:69], 2, s[36:37]
	global_store_dword v[70:71], v50, off
	global_store_dword v[68:69], v15, off
.LBB0_894:
	s_or_b64 exec, exec, s[0:1]
	v_cndmask_b32_e64 v70, 0, 1, s[22:23]
	v_add_u32_e32 v68, s28, v50
	v_ashrrev_i32_e32 v69, 31, v68
	v_add_u32_e32 v14, v14, v70
	v_lshlrev_b64 v[68:69], 6, v[68:69]
	v_cmp_lt_i32_e32 vcc, v14, v17
	v_cndmask_b32_e64 v15, 0, 1, s[96:97]
	v_lshl_add_u64 v[68:69], s[26:27], 0, v[68:69]
	s_and_b64 s[0:1], s[94:95], vcc
	v_cmp_ne_u32_e64 s[100:101], -1, v12
	s_nop 1
	v_cndmask_b32_e64 v254, v252, v68, s[100:101]
	v_cndmask_b32_e64 v255, v253, v69, s[100:101]
	global_store_dword v[254:255], v12, off
	v_add_u32_e32 v13, v13, v15
	s_or_b64 s[2:3], s[92:93], s[0:1]
	v_mov_b32_e32 v12, -1
	v_mov_b32_e32 v15, -1
	s_and_saveexec_b64 s[0:1], s[2:3]
	s_cbranch_execz .LBB0_896
	v_min_i32_e32 v15, v14, v17
	v_add_u32_e32 v15, v15, v13
	v_add_u32_e32 v68, s33, v15
	v_ashrrev_i32_e32 v69, 31, v68
	v_lshlrev_b64 v[68:69], 2, v[68:69]
	v_lshl_add_u64 v[70:71], s[30:31], 0, v[68:69]
	v_lshl_add_u64 v[68:69], s[34:35], 0, v[68:69]
	global_store_dword v[68:69], v8, off
	v_add_u32_e32 v68, s44, v15
	v_ashrrev_i32_e32 v69, 31, v68
	v_lshl_add_u64 v[68:69], v[68:69], 2, s[36:37]
	global_store_dword v[70:71], v51, off
	global_store_dword v[68:69], v8, off
.LBB0_896:
	s_or_b64 exec, exec, s[0:1]
	v_add_u32_e32 v68, s28, v51
	v_add_u32_e32 v8, v13, v66
	v_add_u32_e32 v13, v14, v67
	v_ashrrev_i32_e32 v69, 31, v68
	v_cmp_lt_i32_e32 vcc, v13, v17
	v_lshlrev_b64 v[68:69], 6, v[68:69]
	s_and_b64 s[0:1], s[90:91], vcc
	v_lshl_add_u64 v[68:69], s[26:27], 0, v[68:69]
	s_or_b64 s[2:3], s[88:89], s[0:1]
	v_cmp_ne_u32_e64 s[100:101], -1, v15
	s_nop 1
	v_cndmask_b32_e64 v254, v252, v68, s[100:101]
	v_cndmask_b32_e64 v255, v253, v69, s[100:101]
	global_store_dword v[254:255], v15, off
	s_and_saveexec_b64 s[0:1], s[2:3]
	s_cbranch_execz .LBB0_898
	v_min_i32_e32 v12, v13, v17
	v_add_u32_e32 v12, v12, v8
	v_add_u32_e32 v14, s33, v12
	v_ashrrev_i32_e32 v15, 31, v14
	v_lshlrev_b64 v[14:15], 2, v[14:15]
	v_lshl_add_u64 v[66:67], s[30:31], 0, v[14:15]
	v_lshl_add_u64 v[14:15], s[34:35], 0, v[14:15]
	global_store_dword v[14:15], v9, off
	v_add_u32_e32 v14, s44, v12
	v_ashrrev_i32_e32 v15, 31, v14
	v_lshl_add_u64 v[14:15], v[14:15], 2, s[36:37]
	global_store_dword v[66:67], v52, off
	global_store_dword v[14:15], v9, off
.LBB0_898:
	s_or_b64 exec, exec, s[0:1]
	v_add_u32_e32 v14, s28, v52
	v_ashrrev_i32_e32 v15, 31, v14
	v_lshlrev_b64 v[14:15], 6, v[14:15]
	v_cndmask_b32_e64 v66, 0, 1, s[90:91]
	v_lshl_add_u64 v[14:15], s[26:27], 0, v[14:15]
	v_cmp_ne_u32_e64 s[100:101], -1, v12
	s_nop 1
	v_cndmask_b32_e64 v254, v252, v14, s[100:101]
	v_cndmask_b32_e64 v255, v253, v15, s[100:101]
	global_store_dword v[254:255], v12, off
	v_add_u32_e32 v12, v13, v66
	v_cmp_lt_i32_e32 vcc, v12, v17
	v_cndmask_b32_e64 v9, 0, 1, s[88:89]
	s_and_b64 s[0:1], s[86:87], vcc
	v_add_u32_e32 v9, v8, v9
	s_or_b64 s[2:3], s[84:85], s[0:1]
	v_mov_b32_e32 v8, -1
	v_mov_b32_e32 v13, -1
	s_and_saveexec_b64 s[0:1], s[2:3]
	s_cbranch_execz .LBB0_900
	v_min_i32_e32 v13, v12, v17
	v_add_u32_e32 v13, v13, v9
	v_add_u32_e32 v14, s33, v13
	v_ashrrev_i32_e32 v15, 31, v14
	v_lshlrev_b64 v[14:15], 2, v[14:15]
	v_lshl_add_u64 v[66:67], s[30:31], 0, v[14:15]
	v_lshl_add_u64 v[14:15], s[34:35], 0, v[14:15]
	global_store_dword v[14:15], v10, off
	v_add_u32_e32 v14, s44, v13
	v_ashrrev_i32_e32 v15, 31, v14
	v_lshl_add_u64 v[14:15], v[14:15], 2, s[36:37]
	global_store_dword v[66:67], v53, off
	global_store_dword v[14:15], v10, off
.LBB0_900:
	s_or_b64 exec, exec, s[0:1]
	v_add_u32_e32 v14, s28, v53
	v_add_u32_e32 v10, v12, v65
	v_ashrrev_i32_e32 v15, 31, v14
	v_cmp_lt_i32_e32 vcc, v10, v17
	v_lshlrev_b64 v[14:15], 6, v[14:15]
	s_and_b64 s[0:1], s[82:83], vcc
	v_lshl_add_u64 v[14:15], s[26:27], 0, v[14:15]
	v_add_u32_e32 v9, v9, v33
	s_or_b64 s[2:3], s[80:81], s[0:1]
	v_cmp_ne_u32_e64 s[100:101], -1, v13
	s_nop 1
	v_cndmask_b32_e64 v254, v252, v14, s[100:101]
	v_cndmask_b32_e64 v255, v253, v15, s[100:101]
	global_store_dword v[254:255], v13, off
	s_and_saveexec_b64 s[0:1], s[2:3]
	s_cbranch_execz .LBB0_902
	v_min_i32_e32 v8, v10, v17
	v_add_u32_e32 v8, v8, v9
	v_add_u32_e32 v12, s33, v8
	v_ashrrev_i32_e32 v13, 31, v12
	v_lshlrev_b64 v[12:13], 2, v[12:13]
	v_lshl_add_u64 v[14:15], s[30:31], 0, v[12:13]
	v_lshl_add_u64 v[12:13], s[34:35], 0, v[12:13]
	global_store_dword v[12:13], v11, off
	v_add_u32_e32 v12, s44, v8
	v_ashrrev_i32_e32 v13, 31, v12
	v_lshl_add_u64 v[12:13], v[12:13], 2, s[36:37]
	global_store_dword v[14:15], v54, off
	global_store_dword v[12:13], v11, off
.LBB0_902:
	s_or_b64 exec, exec, s[0:1]
	v_cndmask_b32_e64 v14, 0, 1, s[82:83]
	v_add_u32_e32 v12, s28, v54
	v_ashrrev_i32_e32 v13, 31, v12
	v_add_u32_e32 v10, v10, v14
	v_lshlrev_b64 v[12:13], 6, v[12:13]
	v_cmp_lt_i32_e32 vcc, v10, v17
	v_cndmask_b32_e64 v11, 0, 1, s[80:81]
	v_lshl_add_u64 v[12:13], s[26:27], 0, v[12:13]
	s_and_b64 s[0:1], s[78:79], vcc
	v_cmp_ne_u32_e64 s[100:101], -1, v8
	s_nop 1
	v_cndmask_b32_e64 v254, v252, v12, s[100:101]
	v_cndmask_b32_e64 v255, v253, v13, s[100:101]
	global_store_dword v[254:255], v8, off
	v_add_u32_e32 v9, v9, v11
	s_or_b64 s[2:3], s[76:77], s[0:1]
	v_mov_b32_e32 v8, -1
	v_mov_b32_e32 v11, -1
	s_and_saveexec_b64 s[0:1], s[2:3]
	s_cbranch_execz .LBB0_904
	v_min_i32_e32 v11, v10, v17
	v_add_u32_e32 v11, v11, v9
	v_add_u32_e32 v12, s33, v11
	v_ashrrev_i32_e32 v13, 31, v12
	v_lshlrev_b64 v[12:13], 2, v[12:13]
	v_lshl_add_u64 v[14:15], s[30:31], 0, v[12:13]
	v_lshl_add_u64 v[12:13], s[34:35], 0, v[12:13]
	global_store_dword v[12:13], v4, off
	v_add_u32_e32 v12, s44, v11
	v_ashrrev_i32_e32 v13, 31, v12
	v_lshl_add_u64 v[12:13], v[12:13], 2, s[36:37]
	global_store_dword v[14:15], v55, off
	global_store_dword v[12:13], v4, off
.LBB0_904:
	s_or_b64 exec, exec, s[0:1]
	v_add_u32_e32 v12, s28, v55
	v_add_u32_e32 v4, v9, v29
	v_add_u32_e32 v9, v10, v32
	v_ashrrev_i32_e32 v13, 31, v12
	v_cmp_lt_i32_e32 vcc, v9, v17
	v_lshlrev_b64 v[12:13], 6, v[12:13]
	s_and_b64 s[0:1], s[74:75], vcc
	v_lshl_add_u64 v[12:13], s[26:27], 0, v[12:13]
	s_or_b64 s[2:3], s[72:73], s[0:1]
	v_cmp_ne_u32_e64 s[100:101], -1, v11
	s_nop 1
	v_cndmask_b32_e64 v254, v252, v12, s[100:101]
	v_cndmask_b32_e64 v255, v253, v13, s[100:101]
	global_store_dword v[254:255], v11, off
	s_and_saveexec_b64 s[0:1], s[2:3]
	s_cbranch_execz .LBB0_906
	v_min_i32_e32 v8, v9, v17
	v_add_u32_e32 v8, v8, v4
	v_add_u32_e32 v10, s33, v8
	v_ashrrev_i32_e32 v11, 31, v10
	v_lshlrev_b64 v[10:11], 2, v[10:11]
	v_lshl_add_u64 v[12:13], s[30:31], 0, v[10:11]
	v_lshl_add_u64 v[10:11], s[34:35], 0, v[10:11]
	global_store_dword v[10:11], v5, off
	v_add_u32_e32 v10, s44, v8
	v_ashrrev_i32_e32 v11, 31, v10
	v_lshl_add_u64 v[10:11], v[10:11], 2, s[36:37]
	global_store_dword v[12:13], v56, off
	global_store_dword v[10:11], v5, off
.LBB0_906:
	s_or_b64 exec, exec, s[0:1]
	v_add_u32_e32 v10, s28, v56
	v_ashrrev_i32_e32 v11, 31, v10
	v_lshlrev_b64 v[10:11], 6, v[10:11]
	v_cndmask_b32_e64 v12, 0, 1, s[74:75]
	v_lshl_add_u64 v[10:11], s[26:27], 0, v[10:11]
	v_cmp_ne_u32_e64 s[100:101], -1, v8
	s_nop 1
	v_cndmask_b32_e64 v254, v252, v10, s[100:101]
	v_cndmask_b32_e64 v255, v253, v11, s[100:101]
	global_store_dword v[254:255], v8, off
	v_add_u32_e32 v8, v9, v12
	v_cmp_lt_i32_e32 vcc, v8, v17
	v_cndmask_b32_e64 v5, 0, 1, s[72:73]
	s_and_b64 s[0:1], s[70:71], vcc
	v_add_u32_e32 v5, v4, v5
	s_or_b64 s[2:3], s[68:69], s[0:1]
	v_mov_b32_e32 v4, -1
	v_mov_b32_e32 v9, -1
	s_and_saveexec_b64 s[0:1], s[2:3]
	s_cbranch_execz .LBB0_908
	v_min_i32_e32 v9, v8, v17
	v_add_u32_e32 v9, v9, v5
	v_add_u32_e32 v10, s33, v9
	v_ashrrev_i32_e32 v11, 31, v10
	v_lshlrev_b64 v[10:11], 2, v[10:11]
	v_lshl_add_u64 v[12:13], s[30:31], 0, v[10:11]
	v_lshl_add_u64 v[10:11], s[34:35], 0, v[10:11]
	global_store_dword v[10:11], v6, off
	v_add_u32_e32 v10, s44, v9
	v_ashrrev_i32_e32 v11, 31, v10
	v_lshl_add_u64 v[10:11], v[10:11], 2, s[36:37]
	global_store_dword v[12:13], v57, off
	global_store_dword v[10:11], v6, off
.LBB0_908:
	s_or_b64 exec, exec, s[0:1]
	v_add_u32_e32 v10, s28, v57
	v_add_u32_e32 v6, v8, v27
	v_ashrrev_i32_e32 v11, 31, v10
	v_cmp_lt_i32_e32 vcc, v6, v17
	v_lshlrev_b64 v[10:11], 6, v[10:11]
	s_and_b64 s[0:1], s[66:67], vcc
	v_lshl_add_u64 v[10:11], s[26:27], 0, v[10:11]
	v_add_u32_e32 v5, v5, v25
	s_or_b64 s[2:3], s[64:65], s[0:1]
	v_cmp_ne_u32_e64 s[100:101], -1, v9
	s_nop 1
	v_cndmask_b32_e64 v254, v252, v10, s[100:101]
	v_cndmask_b32_e64 v255, v253, v11, s[100:101]
	global_store_dword v[254:255], v9, off
	s_and_saveexec_b64 s[0:1], s[2:3]
	s_cbranch_execz .LBB0_910
	v_min_i32_e32 v4, v6, v17
	v_add_u32_e32 v4, v4, v5
	v_add_u32_e32 v8, s33, v4
	v_ashrrev_i32_e32 v9, 31, v8
	v_lshlrev_b64 v[8:9], 2, v[8:9]
	v_lshl_add_u64 v[10:11], s[30:31], 0, v[8:9]
	v_lshl_add_u64 v[8:9], s[34:35], 0, v[8:9]
	global_store_dword v[8:9], v7, off
	v_add_u32_e32 v8, s44, v4
	v_ashrrev_i32_e32 v9, 31, v8
	v_lshl_add_u64 v[8:9], v[8:9], 2, s[36:37]
	global_store_dword v[10:11], v58, off
	global_store_dword v[8:9], v7, off
.LBB0_910:
	s_or_b64 exec, exec, s[0:1]
	v_cndmask_b32_e64 v10, 0, 1, s[66:67]
	v_add_u32_e32 v8, s28, v58
	v_ashrrev_i32_e32 v9, 31, v8
	v_add_u32_e32 v6, v6, v10
	v_lshlrev_b64 v[8:9], 6, v[8:9]
	v_cmp_lt_i32_e32 vcc, v6, v17
	v_cndmask_b32_e64 v7, 0, 1, s[64:65]
	v_lshl_add_u64 v[8:9], s[26:27], 0, v[8:9]
	s_and_b64 s[0:1], s[62:63], vcc
	v_cmp_ne_u32_e64 s[100:101], -1, v4
	s_nop 1
	v_cndmask_b32_e64 v254, v252, v8, s[100:101]
	v_cndmask_b32_e64 v255, v253, v9, s[100:101]
	global_store_dword v[254:255], v4, off
	v_add_u32_e32 v5, v5, v7
	s_or_b64 s[2:3], s[60:61], s[0:1]
	v_mov_b32_e32 v4, -1
	v_mov_b32_e32 v7, -1
	s_and_saveexec_b64 s[0:1], s[2:3]
	s_cbranch_execz .LBB0_912
	v_min_i32_e32 v7, v6, v17
	v_add_u32_e32 v7, v7, v5
	v_add_u32_e32 v8, s33, v7
	v_ashrrev_i32_e32 v9, 31, v8
	v_lshlrev_b64 v[8:9], 2, v[8:9]
	v_lshl_add_u64 v[10:11], s[30:31], 0, v[8:9]
	v_lshl_add_u64 v[8:9], s[34:35], 0, v[8:9]
	global_store_dword v[8:9], v0, off
	v_add_u32_e32 v8, s44, v7
	v_ashrrev_i32_e32 v9, 31, v8
	v_lshl_add_u64 v[8:9], v[8:9], 2, s[36:37]
	global_store_dword v[10:11], v59, off
	global_store_dword v[8:9], v0, off
.LBB0_912:
	s_or_b64 exec, exec, s[0:1]
	v_add_u32_e32 v8, s28, v59
	v_add_u32_e32 v0, v5, v19
	v_add_u32_e32 v5, v6, v23
	v_ashrrev_i32_e32 v9, 31, v8
	v_cmp_lt_i32_e32 vcc, v5, v17
	v_lshlrev_b64 v[8:9], 6, v[8:9]
	s_and_b64 s[0:1], s[58:59], vcc
	v_lshl_add_u64 v[8:9], s[26:27], 0, v[8:9]
	s_or_b64 s[2:3], s[56:57], s[0:1]
	v_cmp_ne_u32_e64 s[100:101], -1, v7
	s_nop 1
	v_cndmask_b32_e64 v254, v252, v8, s[100:101]
	v_cndmask_b32_e64 v255, v253, v9, s[100:101]
	global_store_dword v[254:255], v7, off
	s_and_saveexec_b64 s[0:1], s[2:3]
	s_cbranch_execz .LBB0_914
	v_min_i32_e32 v4, v5, v17
	v_add_u32_e32 v4, v4, v0
	v_add_u32_e32 v6, s33, v4
	v_ashrrev_i32_e32 v7, 31, v6
	v_lshlrev_b64 v[6:7], 2, v[6:7]
	v_lshl_add_u64 v[8:9], s[30:31], 0, v[6:7]
	v_lshl_add_u64 v[6:7], s[34:35], 0, v[6:7]
	global_store_dword v[6:7], v1, off
	v_add_u32_e32 v6, s44, v4
	v_ashrrev_i32_e32 v7, 31, v6
	v_lshl_add_u64 v[6:7], v[6:7], 2, s[36:37]
	global_store_dword v[8:9], v60, off
	global_store_dword v[6:7], v1, off
.LBB0_914:
	s_or_b64 exec, exec, s[0:1]
	v_add_u32_e32 v6, s28, v60
	v_ashrrev_i32_e32 v7, 31, v6
	v_lshlrev_b64 v[6:7], 6, v[6:7]
	v_cndmask_b32_e64 v8, 0, 1, s[58:59]
	v_lshl_add_u64 v[6:7], s[26:27], 0, v[6:7]
	v_cmp_ne_u32_e64 s[100:101], -1, v4
	s_nop 1
	v_cndmask_b32_e64 v254, v252, v6, s[100:101]
	v_cndmask_b32_e64 v255, v253, v7, s[100:101]
	global_store_dword v[254:255], v4, off
	v_add_u32_e32 v4, v5, v8
	v_cmp_lt_i32_e32 vcc, v4, v17
	v_cndmask_b32_e64 v1, 0, 1, s[56:57]
	s_and_b64 s[0:1], s[54:55], vcc
	v_add_u32_e32 v1, v0, v1
	s_or_b64 s[2:3], s[52:53], s[0:1]
	v_mov_b32_e32 v0, -1
	v_mov_b32_e32 v5, -1
	s_and_saveexec_b64 s[0:1], s[2:3]
	s_cbranch_execz .LBB0_916
	v_min_i32_e32 v5, v4, v17
	v_add_u32_e32 v5, v5, v1
	v_add_u32_e32 v6, s33, v5
	v_ashrrev_i32_e32 v7, 31, v6
	v_lshlrev_b64 v[6:7], 2, v[6:7]
	v_lshl_add_u64 v[8:9], s[30:31], 0, v[6:7]
	v_lshl_add_u64 v[6:7], s[34:35], 0, v[6:7]
	global_store_dword v[6:7], v2, off
	v_add_u32_e32 v6, s44, v5
	v_ashrrev_i32_e32 v7, 31, v6
	v_lshl_add_u64 v[6:7], v[6:7], 2, s[36:37]
	global_store_dword v[8:9], v61, off
	global_store_dword v[6:7], v2, off
.LBB0_916:
	s_or_b64 exec, exec, s[0:1]
	v_add_u32_e32 v6, s28, v61
	v_add_u32_e32 v2, v4, v18
	v_ashrrev_i32_e32 v7, 31, v6
	v_cmp_lt_i32_e32 vcc, v2, v17
	v_lshlrev_b64 v[6:7], 6, v[6:7]
	s_and_b64 s[0:1], s[50:51], vcc
	v_lshl_add_u64 v[6:7], s[26:27], 0, v[6:7]
	s_or_b64 s[2:3], s[48:49], s[0:1]
	v_cmp_ne_u32_e64 s[100:101], -1, v5
	s_nop 1
	v_cndmask_b32_e64 v254, v252, v6, s[100:101]
	v_cndmask_b32_e64 v255, v253, v7, s[100:101]
	global_store_dword v[254:255], v5, off
	s_and_saveexec_b64 s[0:1], s[2:3]
	s_cbranch_execz .LBB0_727
	v_min_i32_e32 v0, v2, v17
	v_add3_u32 v0, v1, v16, v0
	v_add_u32_e32 v4, s33, v0
	v_ashrrev_i32_e32 v5, 31, v4
	v_lshlrev_b64 v[4:5], 2, v[4:5]
	v_lshl_add_u64 v[6:7], s[30:31], 0, v[4:5]
	v_lshl_add_u64 v[4:5], s[34:35], 0, v[4:5]
	global_store_dword v[4:5], v3, off
	v_add_u32_e32 v4, s44, v0
	v_ashrrev_i32_e32 v5, 31, v4
	v_lshl_add_u64 v[4:5], v[4:5], 2, s[36:37]
	global_store_dword v[6:7], v62, off
	global_store_dword v[4:5], v3, off
	s_branch .LBB0_727
